# speedup vs baseline: 1.1352x; 1.0037x over previous
_Z8attn_fwdPKfPKiPf:
	s_load_dwordx4 s[4:7], s[0:1], 0x0
	s_load_dwordx2 s[12:13], s[0:1], 0x10
	v_and_b32_e32 v235, 63, v0
	v_lshrrev_b32_e32 v236, 4, v0
	v_and_b32_e32 v237, 15, v0
	v_readfirstlane_b32 s17, v0
	s_nop 3
	s_lshr_b32 s17, s17, 6
	v_mul_u32_u24_e32 v229, 0x3000, v236
	v_lshl_add_u32 v229, v237, 4, v229
	v_mul_u32_u24_e32 v227, 144, v236
	v_lshl_add_u32 v227, v237, 3, v227
	v_lshlrev_b32_e32 v230, 2, v235
	v_and_b32_e32 v238, 31, v0
	v_bfe_u32 v236, v0, 5, 1
	v_mul_u32_u24_e32 v225, 144, v238
	v_lshl_add_u32 v225, v236, 4, v225
	v_add_u32_e32 v226, 36864, v225
	v_lshlrev_b32_e32 v234, 2, v236
	v_mul_u32_u24_e32 v228, 144, v235
	s_lshl_b32 s31, s17, 4
	s_add_u32 s31, s31, 36864
	v_add_u32_e32 v228, s31, v228
	s_mul_i32 s32, s17, 8704
	s_add_u32 s32, s32, 73728
	v_lshrrev_b32_e32 v231, 4, v235
	v_mul_u32_u24_e32 v239, 144, v231
	v_lshl_add_u32 v239, v237, 3, v239
	v_add_u32_e32 v239, s32, v239
	v_add_u32_e32 v240, s32, v225
	v_mul_u32_u24_e32 v241, 272, v238
	v_lshl_add_u32 v241, v236, 4, v241
	v_add_u32_e32 v241, s32, v241
	v_mul_u32_u24_e32 v242, 272, v231
	v_lshl_add_u32 v242, v237, 4, v242
	v_add_u32_e32 v242, s32, v242
	v_mul_u32_u24_e32 v243, 0x3000, v231
	v_lshl_add_u32 v243, v237, 4, v243
	v_lshlrev_b32_e32 v244, 12, v231
	v_lshl_add_u32 v244, v237, 4, v244
	s_and_b32 s33, s2, 7
	s_lshr_b32 s31, s2, 3
	s_and_b32 s39, s31, 3
	s_lshr_b32 s40, s31, 3
	s_lshr_b32 s41, s31, 2
	s_and_b32 s41, s41, 1
	s_lshl_b32 s33, s33, 1
	s_add_u32 s41, s41, s33
	s_mul_i32 s16, s40, 0x1800000
	s_lshl_b32 s31, s41, 8
	s_add_u32 s16, s16, s31
	s_add_u32 s18, s16, 4096
	s_lshr_b32 s31, s17, 1
	s_lshl_b32 s31, s31, 4
	s_and_b32 s33, s17, 1
	s_lshl_b32 s33, s33, 2
	s_add_u32 s31, s31, s33
	s_mul_i32 s31, s31, 0x3000
	s_add_u32 s19, s16, 8192
	s_add_u32 s19, s19, s31
	s_lshl_b32 s22, s40, 13
	s_lshl_b32 s31, s39, 8
	s_lshl_b32 s33, s17, 5
	s_add_u32 s31, s31, s33
	s_mul_i32 s29, s31, 0x3000
	s_add_u32 s29, s29, s16
	s_lshl_b32 s33, s40, 11
	s_add_u32 s31, s31, s33
	s_lshl_b32 s30, s31, 12
	s_lshl_b32 s31, s41, 8
	s_add_u32 s30, s30, s31
	s_mov_b32 s37, 0x46800000
	s_mov_b32 s38, 0xbf800000
	s_mov_b32 s34, 0x46800000
	s_mov_b32 s35, 0xc6616bcd
	s_mov_b32 s36, 0x3e38aa3b
	s_mov_b32 s23, 0
	s_mov_b32 s27, 0
	s_mov_b32 s42, 0
	s_waitcnt lgkmcnt(0)
	s_mov_b32 s8, s6
	s_and_b32 s9, s7, 0xffff
	s_mov_b32 s10, 0x7fffffff
	s_mov_b32 s11, 0x20000
	s_and_b32 s5, s5, 0xffff
	s_mov_b32 s6, 0x7fffffff
	s_mov_b32 s7, 0x20000
	s_and_b32 s13, s13, 0xffff
	s_mov_b32 s14, 0x7fffffff
	s_mov_b32 s15, 0x20000
	s_add_u32 s31, s18, 0x0
	buffer_load_dwordx4 v[64:67], v229, s[4:7], s31 offen
	s_add_u32 s31, s18, 0x60000
	buffer_load_dwordx4 v[68:71], v229, s[4:7], s31 offen
	s_add_u32 s31, s18, 0xc0000
	buffer_load_dwordx4 v[72:75], v229, s[4:7], s31 offen
	s_add_u32 s31, s18, 0x120000
	buffer_load_dwordx4 v[76:79], v229, s[4:7], s31 offen
	s_add_u32 s31, s19, 0x0
	buffer_load_dword v80, v230, s[4:7], s31 offen
	s_add_u32 s31, s19, 0x3000
	buffer_load_dword v81, v230, s[4:7], s31 offen
	s_add_u32 s31, s19, 0x6000
	buffer_load_dword v82, v230, s[4:7], s31 offen
	s_add_u32 s31, s19, 0x9000
	buffer_load_dword v83, v230, s[4:7], s31 offen
	s_add_u32 s31, s19, 0x18000
	buffer_load_dword v84, v230, s[4:7], s31 offen
	s_add_u32 s31, s19, 0x1b000
	buffer_load_dword v85, v230, s[4:7], s31 offen
	s_add_u32 s31, s19, 0x1e000
	buffer_load_dword v86, v230, s[4:7], s31 offen
	s_add_u32 s31, s19, 0x21000
	buffer_load_dword v87, v230, s[4:7], s31 offen
	s_add_u32 s31, s19, 0xc0000
	buffer_load_dword v88, v230, s[4:7], s31 offen
	s_add_u32 s31, s19, 0xc3000
	buffer_load_dword v89, v230, s[4:7], s31 offen
	s_add_u32 s31, s19, 0xc6000
	buffer_load_dword v90, v230, s[4:7], s31 offen
	s_add_u32 s31, s19, 0xc9000
	buffer_load_dword v91, v230, s[4:7], s31 offen
	s_add_u32 s31, s19, 0xd8000
	buffer_load_dword v92, v230, s[4:7], s31 offen
	s_add_u32 s31, s19, 0xdb000
	buffer_load_dword v93, v230, s[4:7], s31 offen
	s_add_u32 s31, s19, 0xde000
	buffer_load_dword v94, v230, s[4:7], s31 offen
	s_add_u32 s31, s19, 0xe1000
	buffer_load_dword v95, v230, s[4:7], s31 offen
	buffer_load_dword v224, v230, s[8:11], s22 offen
	s_add_u32 s31, s29, 0x0
	buffer_load_dwordx4 v[0:3], v243, s[4:7], s31 offen nt
	s_add_u32 s31, s29, 0xc000
	buffer_load_dwordx4 v[4:7], v243, s[4:7], s31 offen nt
	s_add_u32 s31, s29, 0x18000
	buffer_load_dwordx4 v[8:11], v243, s[4:7], s31 offen nt
	s_add_u32 s31, s29, 0x24000
	buffer_load_dwordx4 v[12:15], v243, s[4:7], s31 offen nt
	s_add_u32 s31, s29, 0x30000
	buffer_load_dwordx4 v[16:19], v243, s[4:7], s31 offen nt
	s_add_u32 s31, s29, 0x3c000
	buffer_load_dwordx4 v[20:23], v243, s[4:7], s31 offen nt
	s_add_u32 s31, s29, 0x48000
	buffer_load_dwordx4 v[24:27], v243, s[4:7], s31 offen nt
	s_add_u32 s31, s29, 0x54000
	buffer_load_dwordx4 v[28:31], v243, s[4:7], s31 offen nt
	s_add_u32 s31, s29, 0xc00000
	buffer_load_dwordx4 v[32:35], v243, s[4:7], s31 offen nt
	s_add_u32 s31, s29, 0xc0c000
	buffer_load_dwordx4 v[36:39], v243, s[4:7], s31 offen nt
	s_add_u32 s31, s29, 0xc18000
	buffer_load_dwordx4 v[40:43], v243, s[4:7], s31 offen nt
	s_add_u32 s31, s29, 0xc24000
	buffer_load_dwordx4 v[44:47], v243, s[4:7], s31 offen nt
	s_add_u32 s31, s29, 0xc30000
	buffer_load_dwordx4 v[48:51], v243, s[4:7], s31 offen nt
	s_add_u32 s31, s29, 0xc3c000
	buffer_load_dwordx4 v[52:55], v243, s[4:7], s31 offen nt
	s_add_u32 s31, s29, 0xc48000
	buffer_load_dwordx4 v[56:59], v243, s[4:7], s31 offen nt
	s_add_u32 s31, s29, 0xc54000
	buffer_load_dwordx4 v[60:63], v243, s[4:7], s31 offen nt
	s_waitcnt vmcnt(16)
	v_cvt_pk_f16_f32 v64, v64, v65
	v_cvt_pk_f16_f32 v65, v66, v67
	ds_write_b64 v227, v[64:65] offset:0
	v_cvt_pk_f16_f32 v68, v68, v69
	v_cvt_pk_f16_f32 v69, v70, v71
	ds_write_b64 v227, v[68:69] offset:4608
	v_cvt_pk_f16_f32 v72, v72, v73
	v_cvt_pk_f16_f32 v73, v74, v75
	ds_write_b64 v227, v[72:73] offset:9216
	v_cvt_pk_f16_f32 v76, v76, v77
	v_cvt_pk_f16_f32 v77, v78, v79
	ds_write_b64 v227, v[76:77] offset:13824
	v_cvt_pk_f16_f32 v80, v80, v81
	v_cvt_pk_f16_f32 v81, v82, v83
	v_cvt_pk_f16_f32 v82, v84, v85
	v_cvt_pk_f16_f32 v83, v86, v87
	ds_write_b128 v228, v[80:83] offset:0
	v_cvt_pk_f16_f32 v88, v88, v89
	v_cvt_pk_f16_f32 v89, v90, v91
	v_cvt_pk_f16_f32 v90, v92, v93
	v_cvt_pk_f16_f32 v91, v94, v95
	ds_write_b128 v228, v[88:91] offset:9216
	s_add_u32 s31, s18, 0x180000
	buffer_load_dwordx4 v[208:211], v229, s[4:7], s31 offen
	s_add_u32 s31, s18, 0x1e0000
	buffer_load_dwordx4 v[212:215], v229, s[4:7], s31 offen
	s_add_u32 s31, s19, 0x180000
	buffer_load_dword v216, v230, s[4:7], s31 offen
	s_add_u32 s31, s19, 0x183000
	buffer_load_dword v217, v230, s[4:7], s31 offen
	s_add_u32 s31, s19, 0x186000
	buffer_load_dword v218, v230, s[4:7], s31 offen
	s_add_u32 s31, s19, 0x189000
	buffer_load_dword v219, v230, s[4:7], s31 offen
	s_add_u32 s31, s19, 0x198000
	buffer_load_dword v220, v230, s[4:7], s31 offen
	s_add_u32 s31, s19, 0x19b000
	buffer_load_dword v221, v230, s[4:7], s31 offen
	s_add_u32 s31, s19, 0x19e000
	buffer_load_dword v222, v230, s[4:7], s31 offen
	s_add_u32 s31, s19, 0x1a1000
	buffer_load_dword v223, v230, s[4:7], s31 offen
	s_waitcnt vmcnt(10)
	v_mul_f32_e32 v0, s36, v0
	v_mul_f32_e32 v1, s36, v1
	v_mul_f32_e32 v2, s36, v2
	v_mul_f32_e32 v3, s36, v3
	v_cvt_pk_f16_f32 v0, v0, v1
	v_cvt_pk_f16_f32 v1, v2, v3
	ds_write_b64 v239, v[0:1] offset:0
	v_mul_f32_e32 v4, s36, v4
	v_mul_f32_e32 v5, s36, v5
	v_mul_f32_e32 v6, s36, v6
	v_mul_f32_e32 v7, s36, v7
	v_cvt_pk_f16_f32 v4, v4, v5
	v_cvt_pk_f16_f32 v5, v6, v7
	ds_write_b64 v239, v[4:5] offset:576
	v_mul_f32_e32 v8, s36, v8
	v_mul_f32_e32 v9, s36, v9
	v_mul_f32_e32 v10, s36, v10
	v_mul_f32_e32 v11, s36, v11
	v_cvt_pk_f16_f32 v8, v8, v9
	v_cvt_pk_f16_f32 v9, v10, v11
	ds_write_b64 v239, v[8:9] offset:1152
	v_mul_f32_e32 v12, s36, v12
	v_mul_f32_e32 v13, s36, v13
	v_mul_f32_e32 v14, s36, v14
	v_mul_f32_e32 v15, s36, v15
	v_cvt_pk_f16_f32 v12, v12, v13
	v_cvt_pk_f16_f32 v13, v14, v15
	ds_write_b64 v239, v[12:13] offset:1728
	v_mul_f32_e32 v16, s36, v16
	v_mul_f32_e32 v17, s36, v17
	v_mul_f32_e32 v18, s36, v18
	v_mul_f32_e32 v19, s36, v19
	v_cvt_pk_f16_f32 v16, v16, v17
	v_cvt_pk_f16_f32 v17, v18, v19
	ds_write_b64 v239, v[16:17] offset:2304
	v_mul_f32_e32 v20, s36, v20
	v_mul_f32_e32 v21, s36, v21
	v_mul_f32_e32 v22, s36, v22
	v_mul_f32_e32 v23, s36, v23
	v_cvt_pk_f16_f32 v20, v20, v21
	v_cvt_pk_f16_f32 v21, v22, v23
	ds_write_b64 v239, v[20:21] offset:2880
	v_mul_f32_e32 v24, s36, v24
	v_mul_f32_e32 v25, s36, v25
	v_mul_f32_e32 v26, s36, v26
	v_mul_f32_e32 v27, s36, v27
	v_cvt_pk_f16_f32 v24, v24, v25
	v_cvt_pk_f16_f32 v25, v26, v27
	ds_write_b64 v239, v[24:25] offset:3456
	v_mul_f32_e32 v28, s36, v28
	v_mul_f32_e32 v29, s36, v29
	v_mul_f32_e32 v30, s36, v30
	v_mul_f32_e32 v31, s36, v31
	v_cvt_pk_f16_f32 v28, v28, v29
	v_cvt_pk_f16_f32 v29, v30, v31
	ds_write_b64 v239, v[28:29] offset:4032
	s_waitcnt lgkmcnt(0)
	ds_read_b128 v[128:131], v240 offset:0
	ds_read_b128 v[132:135], v240 offset:32
	ds_read_b128 v[136:139], v240 offset:64
	ds_read_b128 v[140:143], v240 offset:96
	s_waitcnt lgkmcnt(0)
	v_mul_f32_e32 v32, s36, v32
	v_mul_f32_e32 v33, s36, v33
	v_mul_f32_e32 v34, s36, v34
	v_mul_f32_e32 v35, s36, v35
	v_cvt_pk_f16_f32 v32, v32, v33
	v_cvt_pk_f16_f32 v33, v34, v35
	ds_write_b64 v239, v[32:33] offset:0
	v_mul_f32_e32 v36, s36, v36
	v_mul_f32_e32 v37, s36, v37
	v_mul_f32_e32 v38, s36, v38
	v_mul_f32_e32 v39, s36, v39
	v_cvt_pk_f16_f32 v36, v36, v37
	v_cvt_pk_f16_f32 v37, v38, v39
	ds_write_b64 v239, v[36:37] offset:576
	v_mul_f32_e32 v40, s36, v40
	v_mul_f32_e32 v41, s36, v41
	v_mul_f32_e32 v42, s36, v42
	v_mul_f32_e32 v43, s36, v43
	v_cvt_pk_f16_f32 v40, v40, v41
	v_cvt_pk_f16_f32 v41, v42, v43
	ds_write_b64 v239, v[40:41] offset:1152
	v_mul_f32_e32 v44, s36, v44
	v_mul_f32_e32 v45, s36, v45
	v_mul_f32_e32 v46, s36, v46
	v_mul_f32_e32 v47, s36, v47
	v_cvt_pk_f16_f32 v44, v44, v45
	v_cvt_pk_f16_f32 v45, v46, v47
	ds_write_b64 v239, v[44:45] offset:1728
	v_mul_f32_e32 v48, s36, v48
	v_mul_f32_e32 v49, s36, v49
	v_mul_f32_e32 v50, s36, v50
	v_mul_f32_e32 v51, s36, v51
	v_cvt_pk_f16_f32 v48, v48, v49
	v_cvt_pk_f16_f32 v49, v50, v51
	ds_write_b64 v239, v[48:49] offset:2304
	v_mul_f32_e32 v52, s36, v52
	v_mul_f32_e32 v53, s36, v53
	v_mul_f32_e32 v54, s36, v54
	v_mul_f32_e32 v55, s36, v55
	v_cvt_pk_f16_f32 v52, v52, v53
	v_cvt_pk_f16_f32 v53, v54, v55
	ds_write_b64 v239, v[52:53] offset:2880
	v_mul_f32_e32 v56, s36, v56
	v_mul_f32_e32 v57, s36, v57
	v_mul_f32_e32 v58, s36, v58
	v_mul_f32_e32 v59, s36, v59
	v_cvt_pk_f16_f32 v56, v56, v57
	v_cvt_pk_f16_f32 v57, v58, v59
	ds_write_b64 v239, v[56:57] offset:3456
	v_mul_f32_e32 v60, s36, v60
	v_mul_f32_e32 v61, s36, v61
	v_mul_f32_e32 v62, s36, v62
	v_mul_f32_e32 v63, s36, v63
	v_cvt_pk_f16_f32 v60, v60, v61
	v_cvt_pk_f16_f32 v61, v62, v63
	ds_write_b64 v239, v[60:61] offset:4032
	s_waitcnt lgkmcnt(0)
	ds_read_b128 v[144:147], v240 offset:0
	ds_read_b128 v[148:151], v240 offset:32
	ds_read_b128 v[152:155], v240 offset:64
	ds_read_b128 v[156:159], v240 offset:96
	s_waitcnt lgkmcnt(0)
	s_barrier
	ds_read_b128 v[176:179], v225 offset:0
	ds_read_b128 v[180:183], v225 offset:32
	ds_read_b128 v[184:187], v225 offset:64
	ds_read_b128 v[188:191], v225 offset:96
	ds_read_b128 v[192:195], v225 offset:4608
	ds_read_b128 v[196:199], v225 offset:4640
	ds_read_b128 v[200:203], v225 offset:4672
	ds_read_b128 v[204:207], v225 offset:4704
	s_waitcnt lgkmcnt(0)
	v_cmp_ne_u32_e64 s[20:21], 0, v224
	v_mfma_f32_32x32x16_f16 v[64:79], v[176:179], v[128:131], 0
	v_mfma_f32_32x32x16_f16 v[64:79], v[180:183], v[132:135], v[64:79]
	v_mfma_f32_32x32x16_f16 v[64:79], v[184:187], v[136:139], v[64:79]
	v_mfma_f32_32x32x16_f16 v[64:79], v[188:191], v[140:143], v[64:79]
	v_mfma_f32_32x32x16_f16 v[80:95], v[192:195], v[128:131], 0
	v_mfma_f32_32x32x16_f16 v[80:95], v[196:199], v[132:135], v[80:95]
	v_mfma_f32_32x32x16_f16 v[80:95], v[200:203], v[136:139], v[80:95]
	v_mfma_f32_32x32x16_f16 v[80:95], v[204:207], v[140:143], v[80:95]
	s_nop 15
	s_nop 3
	s_cmp_eq_u64 s[20:21], -1
	s_cbranch_scc1 .Lpro_nomask_A
	v_lshrrev_b32_e64 v235, v234, s20
	v_bfe_u32 v236, v235, 0, 1
	v_cvt_f32_u32_e32 v236, v236
	v_sub_f32_e32 v236, 1.0, v236
	v_fmac_f32_e32 v64, s35, v236
	v_bfe_u32 v236, v235, 1, 1
	v_cvt_f32_u32_e32 v236, v236
	v_sub_f32_e32 v236, 1.0, v236
	v_fmac_f32_e32 v65, s35, v236
	v_bfe_u32 v236, v235, 2, 1
	v_cvt_f32_u32_e32 v236, v236
	v_sub_f32_e32 v236, 1.0, v236
	v_fmac_f32_e32 v66, s35, v236
	v_bfe_u32 v236, v235, 3, 1
	v_cvt_f32_u32_e32 v236, v236
	v_sub_f32_e32 v236, 1.0, v236
	v_fmac_f32_e32 v67, s35, v236
	v_bfe_u32 v236, v235, 8, 1
	v_cvt_f32_u32_e32 v236, v236
	v_sub_f32_e32 v236, 1.0, v236
	v_fmac_f32_e32 v68, s35, v236
	v_bfe_u32 v236, v235, 9, 1
	v_cvt_f32_u32_e32 v236, v236
	v_sub_f32_e32 v236, 1.0, v236
	v_fmac_f32_e32 v69, s35, v236
	v_bfe_u32 v236, v235, 10, 1
	v_cvt_f32_u32_e32 v236, v236
	v_sub_f32_e32 v236, 1.0, v236
	v_fmac_f32_e32 v70, s35, v236
	v_bfe_u32 v236, v235, 11, 1
	v_cvt_f32_u32_e32 v236, v236
	v_sub_f32_e32 v236, 1.0, v236
	v_fmac_f32_e32 v71, s35, v236
	v_bfe_u32 v236, v235, 16, 1
	v_cvt_f32_u32_e32 v236, v236
	v_sub_f32_e32 v236, 1.0, v236
	v_fmac_f32_e32 v72, s35, v236
	v_bfe_u32 v236, v235, 17, 1
	v_cvt_f32_u32_e32 v236, v236
	v_sub_f32_e32 v236, 1.0, v236
	v_fmac_f32_e32 v73, s35, v236
	v_bfe_u32 v236, v235, 18, 1
	v_cvt_f32_u32_e32 v236, v236
	v_sub_f32_e32 v236, 1.0, v236
	v_fmac_f32_e32 v74, s35, v236
	v_bfe_u32 v236, v235, 19, 1
	v_cvt_f32_u32_e32 v236, v236
	v_sub_f32_e32 v236, 1.0, v236
	v_fmac_f32_e32 v75, s35, v236
	v_bfe_u32 v236, v235, 24, 1
	v_cvt_f32_u32_e32 v236, v236
	v_sub_f32_e32 v236, 1.0, v236
	v_fmac_f32_e32 v76, s35, v236
	v_bfe_u32 v236, v235, 25, 1
	v_cvt_f32_u32_e32 v236, v236
	v_sub_f32_e32 v236, 1.0, v236
	v_fmac_f32_e32 v77, s35, v236
	v_bfe_u32 v236, v235, 26, 1
	v_cvt_f32_u32_e32 v236, v236
	v_sub_f32_e32 v236, 1.0, v236
	v_fmac_f32_e32 v78, s35, v236
	v_bfe_u32 v236, v235, 27, 1
	v_cvt_f32_u32_e32 v236, v236
	v_sub_f32_e32 v236, 1.0, v236
	v_fmac_f32_e32 v79, s35, v236
	v_lshrrev_b32_e64 v235, v234, s21
	v_bfe_u32 v236, v235, 0, 1
	v_cvt_f32_u32_e32 v236, v236
	v_sub_f32_e32 v236, 1.0, v236
	v_fmac_f32_e32 v80, s35, v236
	v_bfe_u32 v236, v235, 1, 1
	v_cvt_f32_u32_e32 v236, v236
	v_sub_f32_e32 v236, 1.0, v236
	v_fmac_f32_e32 v81, s35, v236
	v_bfe_u32 v236, v235, 2, 1
	v_cvt_f32_u32_e32 v236, v236
	v_sub_f32_e32 v236, 1.0, v236
	v_fmac_f32_e32 v82, s35, v236
	v_bfe_u32 v236, v235, 3, 1
	v_cvt_f32_u32_e32 v236, v236
	v_sub_f32_e32 v236, 1.0, v236
	v_fmac_f32_e32 v83, s35, v236
	v_bfe_u32 v236, v235, 8, 1
	v_cvt_f32_u32_e32 v236, v236
	v_sub_f32_e32 v236, 1.0, v236
	v_fmac_f32_e32 v84, s35, v236
	v_bfe_u32 v236, v235, 9, 1
	v_cvt_f32_u32_e32 v236, v236
	v_sub_f32_e32 v236, 1.0, v236
	v_fmac_f32_e32 v85, s35, v236
	v_bfe_u32 v236, v235, 10, 1
	v_cvt_f32_u32_e32 v236, v236
	v_sub_f32_e32 v236, 1.0, v236
	v_fmac_f32_e32 v86, s35, v236
	v_bfe_u32 v236, v235, 11, 1
	v_cvt_f32_u32_e32 v236, v236
	v_sub_f32_e32 v236, 1.0, v236
	v_fmac_f32_e32 v87, s35, v236
	v_bfe_u32 v236, v235, 16, 1
	v_cvt_f32_u32_e32 v236, v236
	v_sub_f32_e32 v236, 1.0, v236
	v_fmac_f32_e32 v88, s35, v236
	v_bfe_u32 v236, v235, 17, 1
	v_cvt_f32_u32_e32 v236, v236
	v_sub_f32_e32 v236, 1.0, v236
	v_fmac_f32_e32 v89, s35, v236
	v_bfe_u32 v236, v235, 18, 1
	v_cvt_f32_u32_e32 v236, v236
	v_sub_f32_e32 v236, 1.0, v236
	v_fmac_f32_e32 v90, s35, v236
	v_bfe_u32 v236, v235, 19, 1
	v_cvt_f32_u32_e32 v236, v236
	v_sub_f32_e32 v236, 1.0, v236
	v_fmac_f32_e32 v91, s35, v236
	v_bfe_u32 v236, v235, 24, 1
	v_cvt_f32_u32_e32 v236, v236
	v_sub_f32_e32 v236, 1.0, v236
	v_fmac_f32_e32 v92, s35, v236
	v_bfe_u32 v236, v235, 25, 1
	v_cvt_f32_u32_e32 v236, v236
	v_sub_f32_e32 v236, 1.0, v236
	v_fmac_f32_e32 v93, s35, v236
	v_bfe_u32 v236, v235, 26, 1
	v_cvt_f32_u32_e32 v236, v236
	v_sub_f32_e32 v236, 1.0, v236
	v_fmac_f32_e32 v94, s35, v236
	v_bfe_u32 v236, v235, 27, 1
	v_cvt_f32_u32_e32 v236, v236
	v_sub_f32_e32 v236, 1.0, v236
	v_fmac_f32_e32 v95, s35, v236

.Lpro_nomask_B:
	v_max3_f32 v235, v160, v161, v162
	v_max3_f32 v235, v235, v163, v164
	v_max3_f32 v235, v235, v165, v166
	v_max3_f32 v235, v235, v167, v168
	v_max3_f32 v235, v235, v169, v170
	v_max3_f32 v235, v235, v171, v172
	v_max3_f32 v235, v235, v173, v174
	v_max3_f32 v235, v235, v175, v80
	v_max3_f32 v235, v235, v81, v82
	v_max3_f32 v235, v235, v83, v84
	v_max3_f32 v235, v235, v85, v86
	v_max3_f32 v235, v235, v87, v88
	v_max3_f32 v235, v235, v89, v90
	v_max3_f32 v235, v235, v91, v92
	v_max3_f32 v235, v235, v93, v94
	v_max_f32_e32 v235, v235, v95
	v_mov_b32_e32 v236, v235
	s_nop 1
	v_permlane32_swap_b32_e32 v235, v236
	v_max_f32_e32 v235, v235, v236
	v_sub_f32_e32 v112, 0, v235
	v_sub_f32_e32 v113, 0, v235
	v_sub_f32_e32 v114, 0, v235
	v_sub_f32_e32 v115, 0, v235
	v_sub_f32_e32 v116, 0, v235
	v_sub_f32_e32 v117, 0, v235
	v_sub_f32_e32 v118, 0, v235
	v_sub_f32_e32 v119, 0, v235
	v_sub_f32_e32 v120, 0, v235
	v_sub_f32_e32 v121, 0, v235
	v_sub_f32_e32 v122, 0, v235
	v_sub_f32_e32 v123, 0, v235
	v_sub_f32_e32 v124, 0, v235
	v_sub_f32_e32 v125, 0, v235
	v_sub_f32_e32 v126, 0, v235
	v_sub_f32_e32 v127, 0, v235
	v_mov_b32_e32 v0, 0
	v_mov_b32_e32 v1, 0
	v_mov_b32_e32 v2, 0
	v_mov_b32_e32 v3, 0
	v_mov_b32_e32 v4, 0
	v_mov_b32_e32 v5, 0
	v_mov_b32_e32 v6, 0
	v_mov_b32_e32 v7, 0
	v_mov_b32_e32 v8, 0
	v_mov_b32_e32 v9, 0
	v_mov_b32_e32 v10, 0
	v_mov_b32_e32 v11, 0
	v_mov_b32_e32 v12, 0
	v_mov_b32_e32 v13, 0
	v_mov_b32_e32 v14, 0
	v_mov_b32_e32 v15, 0
	v_mov_b32_e32 v16, 0
	v_mov_b32_e32 v17, 0
	v_mov_b32_e32 v18, 0
	v_mov_b32_e32 v19, 0
	v_mov_b32_e32 v20, 0
	v_mov_b32_e32 v21, 0
	v_mov_b32_e32 v22, 0
	v_mov_b32_e32 v23, 0
	v_mov_b32_e32 v24, 0
	v_mov_b32_e32 v25, 0
	v_mov_b32_e32 v26, 0
	v_mov_b32_e32 v27, 0
	v_mov_b32_e32 v28, 0
	v_mov_b32_e32 v29, 0
	v_mov_b32_e32 v30, 0
	v_mov_b32_e32 v31, 0
	v_mov_b32_e32 v32, 0
	v_mov_b32_e32 v33, 0
	v_mov_b32_e32 v34, 0
	v_mov_b32_e32 v35, 0
	v_mov_b32_e32 v36, 0
	v_mov_b32_e32 v37, 0
	v_mov_b32_e32 v38, 0
	v_mov_b32_e32 v39, 0
	v_mov_b32_e32 v40, 0
	v_mov_b32_e32 v41, 0
	v_mov_b32_e32 v42, 0
	v_mov_b32_e32 v43, 0
	v_mov_b32_e32 v44, 0
	v_mov_b32_e32 v45, 0
	v_mov_b32_e32 v46, 0
	v_mov_b32_e32 v47, 0
	v_mov_b32_e32 v48, 0
	v_mov_b32_e32 v49, 0
	v_mov_b32_e32 v50, 0
	v_mov_b32_e32 v51, 0
	v_mov_b32_e32 v52, 0
	v_mov_b32_e32 v53, 0
	v_mov_b32_e32 v54, 0
	v_mov_b32_e32 v55, 0
	v_mov_b32_e32 v56, 0
	v_mov_b32_e32 v57, 0
	v_mov_b32_e32 v58, 0
	v_mov_b32_e32 v59, 0
	v_mov_b32_e32 v60, 0
	v_mov_b32_e32 v61, 0
	v_mov_b32_e32 v62, 0
	v_mov_b32_e32 v63, 0
	v_mov_b32_e32 v168, 0
	v_mov_b32_e32 v169, 0
	v_mov_b32_e32 v170, 0
	v_mov_b32_e32 v171, 0
	v_mov_b32_e32 v172, 0
	v_mov_b32_e32 v173, 0
	v_mov_b32_e32 v174, 0
	v_mov_b32_e32 v175, 0
	v_mov_b32_e32 v232, 0
	v_mov_b32_e32 v233, 0
	s_cmp_lt_u32 s17, 4
	s_cbranch_scc1 .Lnoprio
	s_setprio 1
.Lnoprio:
.Lbody:
	s_waitcnt vmcnt(8)
	v_cmp_ne_u32_e64 s[20:21], 0, v224
	s_add_u32 s31, s23, 1
	s_and_b32 s31, s31, 31
	s_lshl_b32 s31, s31, 8
	s_add_u32 s26, s31, s22
	s_add_u32 s31, s23, 3
	s_and_b32 s31, s31, 31
	s_mul_i32 s31, s31, 0xc0000
	s_add_u32 s24, s31, s18
	s_add_u32 s25, s31, s19
	s_cmp_eq_u64 s[20:21], -1
	s_cselect_b32 s34, s37, s38
	s_waitcnt lgkmcnt(4)
	v_mfma_f32_32x32x16_f16 v[80:95], v[176:179], v[144:147], v[112:127]
	ds_read_b128 v[176:179], v225 offset:4608
	v_exp_f32_e32 v64, v64
	v_exp_f32_e32 v65, v65
	buffer_load_dword v224, v230, s[8:11], s26 offen
	v_cvt_pk_f16_f32 v208, v208, v209
	v_cvt_pk_f16_f32 v209, v210, v211
	v_mfma_f32_32x32x16_f16 v[80:95], v[180:183], v[148:151], v[80:95]
	ds_read_b128 v[180:183], v225 offset:4640
	v_exp_f32_e32 v66, v66
	v_exp_f32_e32 v67, v67
	v_cvt_pk_f16_f32 v212, v212, v213
	v_cvt_pk_f16_f32 v160, v64, v65
	v_add_f32_e32 v64, v64, v65
	v_cvt_pk_f16_f32 v213, v214, v215
	v_mfma_f32_32x32x16_f16 v[80:95], v[184:187], v[152:155], v[80:95]
	ds_write_b64 v227, v[208:209] offset:18432
	ds_write_b64 v227, v[212:213] offset:23040
	ds_read_b128 v[184:187], v225 offset:4672
	v_exp_f32_e32 v68, v68
	v_exp_f32_e32 v69, v69
	v_cvt_pk_f16_f32 v161, v66, v67
	v_add_f32_e32 v66, v66, v67
	v_mfma_f32_32x32x16_f16 v[80:95], v[188:191], v[156:159], v[80:95]
	ds_read_b128 v[188:191], v225 offset:4704
	v_exp_f32_e32 v70, v70
	v_exp_f32_e32 v71, v71
	v_cvt_pk_f16_f32 v162, v68, v69
	v_add_f32_e32 v68, v68, v69
	v_add_f32_e32 v231, v64, v66
	s_waitcnt lgkmcnt(6)
	v_mfma_f32_32x32x16_f16 v[32:47], v[192:195], v[168:171], v[32:47]
	ds_read_b128 v[192:195], v226 offset:0
	v_exp_f32_e32 v72, v72
	v_exp_f32_e32 v73, v73
	v_cvt_pk_f16_f32 v163, v70, v71
	v_add_f32_e32 v70, v70, v71
	v_add_f32_e32 v231, v231, v68
	v_mfma_f32_32x32x16_f16 v[48:63], v[196:199], v[168:171], v[48:63]
	ds_read_b128 v[196:199], v226 offset:4608
	v_exp_f32_e32 v74, v74
	v_exp_f32_e32 v75, v75
	v_cvt_pk_f16_f32 v164, v72, v73
	v_add_f32_e32 v72, v72, v73
	v_add_f32_e32 v231, v231, v70
	v_mfma_f32_32x32x16_f16 v[32:47], v[200:203], v[172:175], v[32:47]
	ds_read_b128 v[200:203], v226 offset:32
	v_exp_f32_e32 v76, v76
	v_exp_f32_e32 v77, v77
	v_cvt_pk_f16_f32 v165, v74, v75
	v_add_f32_e32 v74, v74, v75
	v_add_f32_e32 v231, v231, v72
	v_mfma_f32_32x32x16_f16 v[48:63], v[204:207], v[172:175], v[48:63]
	ds_read_b128 v[204:207], v226 offset:4640
	v_exp_f32_e32 v78, v78
	v_exp_f32_e32 v79, v79
	v_cvt_pk_f16_f32 v166, v76, v77
	v_add_f32_e32 v76, v76, v77
	v_add_f32_e32 v231, v231, v74
	v_cvt_pk_f16_f32 v167, v78, v79
	v_add_f32_e32 v78, v78, v79
	v_add_f32_e32 v231, v231, v76
	v_add_f32_e32 v231, v231, v78
	v_cmp_nge_f32_e32 vcc, s34, v231
	s_cbranch_vccnz .Lovf_a00

	.amdhsa_kernel _Z8attn_fwdPKfPKiPf
		.amdhsa_group_segment_fixed_size 143360
		.amdhsa_private_segment_fixed_size 0
		.amdhsa_kernarg_size 24
		.amdhsa_user_sgpr_count 2
		.amdhsa_user_sgpr_dispatch_ptr 0
		.amdhsa_user_sgpr_queue_ptr 0
		.amdhsa_user_sgpr_kernarg_segment_ptr 1
		.amdhsa_user_sgpr_dispatch_id 0
		.amdhsa_user_sgpr_kernarg_preload_length 0
		.amdhsa_user_sgpr_kernarg_preload_offset 0
		.amdhsa_user_sgpr_private_segment_size 0
		.amdhsa_uses_dynamic_stack 0
		.amdhsa_enable_private_segment 0
		.amdhsa_system_sgpr_workgroup_id_x 1
		.amdhsa_system_sgpr_workgroup_id_y 0
		.amdhsa_system_sgpr_workgroup_id_z 0
		.amdhsa_system_sgpr_workgroup_info 0
		.amdhsa_system_vgpr_workitem_id 0
		.amdhsa_next_free_vgpr 248
		.amdhsa_next_free_sgpr 56
		.amdhsa_accum_offset 248
		.amdhsa_reserve_vcc 1
		.amdhsa_float_round_mode_32 0
		.amdhsa_float_round_mode_16_64 0
		.amdhsa_float_denorm_mode_32 3
		.amdhsa_float_denorm_mode_16_64 3
		.amdhsa_dx10_clamp 1
		.amdhsa_ieee_mode 1
		.amdhsa_fp16_overflow 0
		.amdhsa_tg_split 0
		.amdhsa_exception_fp_ieee_invalid_op 0
		.amdhsa_exception_fp_denorm_src 0
		.amdhsa_exception_fp_ieee_div_zero 0
		.amdhsa_exception_fp_ieee_overflow 0
		.amdhsa_exception_fp_ieee_underflow 0
		.amdhsa_exception_fp_ieee_inexact 0
		.amdhsa_exception_int_div_zero 0
	.end_amdhsa_kernel

.Lfunc_end0:
	.size	_Z8attn_fwdPKfPKiPf, .Lfunc_end0-_Z8attn_fwdPKfPKiPf
	.set _Z8attn_fwdPKfPKiPf.num_vgpr, 248
	.set _Z8attn_fwdPKfPKiPf.num_agpr, 0
	.set _Z8attn_fwdPKfPKiPf.numbered_sgpr, 56
	.set _Z8attn_fwdPKfPKiPf.num_named_barrier, 0
	.set _Z8attn_fwdPKfPKiPf.private_seg_size, 0
	.set _Z8attn_fwdPKfPKiPf.uses_vcc, 1
	.set _Z8attn_fwdPKfPKiPf.uses_flat_scratch, 0
	.set _Z8attn_fwdPKfPKiPf.has_dyn_sized_stack, 0
	.set _Z8attn_fwdPKfPKiPf.has_recursion, 0
	.set _Z8attn_fwdPKfPKiPf.has_indirect_call, 0

amdhsa.kernels:
  - .agpr_count:     0
    .args:
      - .actual_access:  read_only
        .address_space:  global
        .offset:         0
        .size:           8
        .value_kind:     global_buffer
      - .actual_access:  read_only
        .address_space:  global
        .offset:         8
        .size:           8
        .value_kind:     global_buffer
      - .actual_access:  write_only
        .address_space:  global
        .offset:         16
        .size:           8
        .value_kind:     global_buffer
    .group_segment_fixed_size: 143360
    .kernarg_segment_align: 8
    .kernarg_segment_size: 24
    .language:       OpenCL C
    .language_version:
      - 2
      - 0
    .max_flat_workgroup_size: 512
    .name:           _Z8attn_fwdPKfPKiPf
    .private_segment_fixed_size: 0
    .sgpr_count:     62
    .sgpr_spill_count: 0
    .symbol:         _Z8attn_fwdPKfPKiPf.kd
    .uniform_work_group_size: 1
    .uses_dynamic_stack: false
    .vgpr_count:     248
    .vgpr_spill_count: 0
    .wavefront_size: 64
